# P0: item split between the adaLN workgroups and the others rebalanced (2.5 vs 3 items per wave) after the mod GEMV got faster
# speedup vs baseline: 1.0000x; 1.0000x over previous
; __device__ __forceinline__ void p0_prologue(const Args& a, const Frame& F) {
;     ...
;     const int nmodb = F.G < 96 ? F.G : 96, nwn = (F.G - nmodb) * 8, nfirst = 3 * nwn < NITEMS ? 3 * nwn : NITEMS;
;     const bool modb = F.bid < nmodb;
;     const int it0 = modb ? nfirst + F.bid * 8 + F.wave : (F.bid - nmodb) * 8 + F.wave, itend = modb ? NITEMS : nfirst, itstep = modb ? nmodb * 8 : nwn;
.LBB0_18:
	s_min_i32 s4, s3, 0x60
	s_sub_i32 s5, s3, s4
	s_cmpk_lt_i32 s5, 0xae
	s_mul_i32 s0, s5, 20
	s_cselect_b32 s76, s0, 0x1040
	s_cmp_ge_i32 s2, s4
	s_waitcnt lgkmcnt(0)
	s_barrier
	s_cbranch_scc0 .LBB0_21
	s_sub_i32 s0, s2, s4
	s_lshl_b32 s0, s0, 3
	s_add_i32 s77, s0, s96
	s_cbranch_execz .LBB0_22
	s_mov_b32 s4, s5
	s_cmp_ge_i32 s77, s76
	s_cbranch_scc0 .LBB0_23
	s_branch .LBB0_112
